# scanner chunk loop: compact incremental loop header (ring offset / first row of next chunk) replaces the compiler's per-chunk recomputation
# speedup vs baseline: 1.0041x; 1.0041x over previous
.LBB0_604:
	s_ashr_i32 s1, s57, 2
	s_and_b32 s0, s57, 7
	s_and_b32 s1, s1, -8
	s_or_b32 s0, s1, s0
	s_ashr_i32 s1, s0, 1
	s_lshr_b32 s6, s1, 30
	s_add_i32 s6, s1, s6
	s_and_b32 s6, s6, -4
	s_waitcnt lgkmcnt(0)
	s_sub_i32 s51, s1, s6
	s_ashr_i32 s1, s57, 31
	s_lshr_b32 s1, s1, 29
	s_add_i32 s0, s0, s1
	s_bfe_u32 s7, s57, 0x20003
	s_and_b32 s50, s57, 1
	s_ashr_i32 s6, s0, 3
	s_mov_b64 s[0:1], -1
	s_and_b64 vcc, exec, s[64:65]
	s_barrier
	s_cbranch_vccz .LBB0_617
	s_load_dwordx2 s[0:1], s[58:59], 0x1e8
	s_mul_i32 s8, s50, 0x1100000
	v_mov_b32_e32 v14, 0
	v_bfrev_b32_e32 v89, v85
	v_and_b32_e32 v112, 2, v85
	v_and_b32_e32 v113, 1, v85
	v_lshrrev_b32_e32 v89, 28, v89
	v_cmp_ne_u32_e64 s[14:15], 0, v112
	v_cmp_ne_u32_e64 s[16:17], 0, v113
	v_or_b32_e32 v94, 16, v89
	s_cmp_lg_u32 s50, 0
	s_cselect_b32 s20, -32, 32
	s_cselect_b32 s21, 0xfff, 0
	s_lshl_b32 s22, s6, 12
	s_add_i32 s21, s21, s22
	v_mov_b32_e32 v15, v14
	v_mov_b32_e32 v16, v14
	s_waitcnt lgkmcnt(0)
	s_add_u32 s8, s0, s8
	s_addc_u32 s9, s1, 0
	s_lshl_b32 s0, s51, 6
	s_ashr_i32 s1, s0, 31
	s_lshl_b64 s[0:1], s[0:1], 1
	s_add_u32 s0, s8, s0
	s_addc_u32 s1, s9, s1
	s_lshl_b32 s8, s7, 5
	s_add_u32 s0, s0, s8
	s_addc_u32 s1, s1, 0
	s_cmp_lg_u32 s50, 0
	v_lshl_add_u64 v[10:11], v[82:83], 1, s[0:1]
	s_cselect_b64 s[0:1], -1, 0
	s_lshl_b32 s70, s6, 12
	s_lshl_b32 s33, s6, 8
	s_mov_b32 s8, 0
	s_add_i32 s9, s70, 0x10ff
	s_add_i32 s52, s33, 0x80ff
	s_addk_i32 s70, 0xff00
	s_add_i32 s71, s33, 0x8000
	v_mov_b32_e32 v17, v14
	s_barrier
	v_mov_b32_e32 v18, v87
	v_add_u32_e32 v2, 0xa000, v96
	ds_read_b128 v[20:23], v18
	ds_read_b128 v[28:31], v18 offset:24576
	ds_read2_b32 v[120:121], v2 offset1:16
	ds_read_b128 v[24:27], v18 offset:8192
	ds_read_b128 v[32:35], v18 offset:32768
	ds_read_b128 v[36:39], v18 offset:256
	ds_read_b128 v[44:47], v18 offset:24832
	ds_read_b128 v[40:43], v18 offset:8448
	ds_read_b128 v[48:51], v18 offset:33024
	s_branch .LBB0_608

.LBB0_607:
	s_mul_i32 s33, s8, 0xab
	s_bfe_u32 s33, s33, 0x70009
	s_mul_i32 s33, s33, 3
	s_sub_i32 s33, s8, s33
	s_and_b32 s33, s33, 0xff
	s_mul_i32 s33, s33, 0xa800
	s_add_i32 s33, s33, 0
	s_mov_b32 s19, s46
.Lsc_body:
	s_waitcnt vmcnt(0)
	s_add_i32 s18, s33, 0xa800
	s_cmp_eq_u32 s18, 0x1f800
	s_cselect_b32 s18, 0, s18
	s_ashr_i32 s47, s46, 31
	s_lshl_b64 s[46:47], s[46:47], 9
	v_add_u32_e32 v18, s33, v87
	v_add_u32_e32 v19, s33, v96
	v_add_u32_e32 v68, s18, v87
	v_add_u32_e32 v69, s18, v96
	v_add_u32_e32 v2, 0xa000, v19
	v_add_u32_e32 v3, 0xa400, v19
	v_add_u32_e32 v69, 0xa000, v69
	s_waitcnt lgkmcnt(5)
	v_pk_mul_f32 v[126:127], v[14:15], v[20:21]
	v_pk_mul_f32 v[128:129], v[14:15], v[112:113]
	v_pk_fma_f32 v[126:127], v[16:17], v[22:23], v[126:127]
	v_pk_fma_f32 v[128:129], v[16:17], v[114:115], v[128:129]
	v_add_f32_e32 v124, v126, v127
	v_pk_fma_f32 v[14:15], v[28:29], v[120:121], v[14:15] op_sel_hi:[1,0,1]
	v_add_f32_e32 v131, v128, v129
	v_add_f32_dpp v124, v124, v124 quad_perm:[1,0,3,2] row_mask:0xf bank_mask:0xf bound_ctrl:1
	v_pk_fma_f32 v[16:17], v[30:31], v[120:121], v[16:17] op_sel_hi:[1,0,1]
	ds_read_b128 v[52:55], v18 offset:512
	v_add_f32_dpp v124, v124, v124 quad_perm:[2,3,0,1] row_mask:0xf bank_mask:0xf bound_ctrl:1
	ds_read_b128 v[60:63], v18 offset:25088
	ds_read2_b32 v[122:123], v2 offset0:32 offset1:48
	v_add_f32_dpp v124, v124, v124 row_half_mirror row_mask:0xf bank_mask:0xf bound_ctrl:1
	ds_read_b128 v[56:59], v18 offset:8704
	ds_read_b128 v[64:67], v18 offset:33280
	v_add_f32_dpp v124, v124, v124 row_mirror row_mask:0xf bank_mask:0xf bound_ctrl:1
	v_pk_fma_f32 v[14:15], v[24:25], v[124:125], v[14:15] op_sel_hi:[1,0,1] neg_lo:[0,1,0] neg_hi:[0,1,0]
	v_pk_fma_f32 v[16:17], v[26:27], v[124:125], v[16:17] op_sel_hi:[1,0,1] neg_lo:[0,1,0] neg_hi:[0,1,0]
	v_add_f32_dpp v133, v130, v130 row_mirror row_mask:0xf bank_mask:0x3 bound_ctrl:1
	s_waitcnt lgkmcnt(6)
	v_pk_mul_f32 v[126:127], v[14:15], v[36:37]
	v_pk_mul_f32 v[128:129], v[14:15], v[32:33]
	v_pk_fma_f32 v[126:127], v[16:17], v[38:39], v[126:127]
	v_pk_fma_f32 v[128:129], v[16:17], v[34:35], v[128:129]
	v_add_f32_e32 v124, v126, v127
	v_pk_fma_f32 v[14:15], v[44:45], v[120:121], v[14:15] op_sel:[0,1,0]
	v_add_f32_e32 v130, v128, v129
	v_add_f32_dpp v124, v124, v124 quad_perm:[1,0,3,2] row_mask:0xf bank_mask:0xf bound_ctrl:1
	v_pk_fma_f32 v[16:17], v[46:47], v[120:121], v[16:17] op_sel:[0,1,0]
	ds_read_b128 v[100:103], v18 offset:768
	v_add_f32_dpp v124, v124, v124 quad_perm:[2,3,0,1] row_mask:0xf bank_mask:0xf bound_ctrl:1
	ds_read_b128 v[108:111], v18 offset:25344
	ds_read_b128 v[116:119], v18 offset:17152
	v_add_f32_dpp v124, v124, v124 row_half_mirror row_mask:0xf bank_mask:0xf bound_ctrl:1
	ds_read_b128 v[104:107], v18 offset:8960
	ds_read_b128 v[112:115], v18 offset:33536
	v_add_f32_dpp v124, v124, v124 row_mirror row_mask:0xf bank_mask:0xf bound_ctrl:1
	v_pk_fma_f32 v[14:15], v[40:41], v[124:125], v[14:15] op_sel_hi:[1,0,1] neg_lo:[0,1,0] neg_hi:[0,1,0]
	v_pk_fma_f32 v[16:17], v[42:43], v[124:125], v[16:17] op_sel_hi:[1,0,1] neg_lo:[0,1,0] neg_hi:[0,1,0]
	v_add_f32_dpp v133, v131, v131 row_mirror row_mask:0xf bank_mask:0xc bound_ctrl:1
	v_add_f32_dpp v135, v132, v132 row_half_mirror row_mask:0xf bank_mask:0x5 bound_ctrl:1
	s_waitcnt lgkmcnt(6)
	v_pk_mul_f32 v[126:127], v[14:15], v[52:53]
	v_pk_mul_f32 v[128:129], v[14:15], v[48:49]
	v_pk_fma_f32 v[126:127], v[16:17], v[54:55], v[126:127]
	v_pk_fma_f32 v[128:129], v[16:17], v[50:51], v[128:129]
	v_add_f32_e32 v124, v126, v127
	v_pk_fma_f32 v[14:15], v[60:61], v[122:123], v[14:15] op_sel_hi:[1,0,1]
	v_add_f32_e32 v131, v128, v129
	v_add_f32_dpp v124, v124, v124 quad_perm:[1,0,3,2] row_mask:0xf bank_mask:0xf bound_ctrl:1
	v_pk_fma_f32 v[16:17], v[62:63], v[122:123], v[16:17] op_sel_hi:[1,0,1]
	ds_read_b128 v[20:23], v18 offset:1024
	v_add_f32_dpp v124, v124, v124 quad_perm:[2,3,0,1] row_mask:0xf bank_mask:0xf bound_ctrl:1
	ds_read_b128 v[28:31], v18 offset:25600
	ds_read2_b32 v[120:121], v2 offset0:64 offset1:80
	v_add_f32_dpp v124, v124, v124 row_half_mirror row_mask:0xf bank_mask:0xf bound_ctrl:1
	ds_read_b128 v[24:27], v18 offset:9216
	ds_read_b128 v[32:35], v18 offset:33792
	v_add_f32_dpp v124, v124, v124 row_mirror row_mask:0xf bank_mask:0xf bound_ctrl:1
	v_pk_fma_f32 v[14:15], v[56:57], v[124:125], v[14:15] op_sel_hi:[1,0,1] neg_lo:[0,1,0] neg_hi:[0,1,0]
	v_pk_fma_f32 v[16:17], v[58:59], v[124:125], v[16:17] op_sel_hi:[1,0,1] neg_lo:[0,1,0] neg_hi:[0,1,0]
	v_lshl_add_u64 v[12:13], v[10:11], 0, s[46:47]
	v_mul_hi_i32_i24_e32 v5, s44, v89
	v_mul_i32_i24_e32 v4, s44, v89
	v_add_f32_dpp v135, v133, v133 row_half_mirror row_mask:0xf bank_mask:0xa bound_ctrl:1
	v_add_f32_dpp v138, v134, v134 quad_perm:[2,3,0,1] row_mask:0xf bank_mask:0xf bound_ctrl:1
	s_nop 0
	v_add_f32_dpp v98, v135, v135 quad_perm:[2,3,0,1] row_mask:0xf bank_mask:0xf bound_ctrl:1
	v_cndmask_b32_e64 v137, v138, v98, s[14:15]
	v_add_f32_dpp v138, v136, v136 quad_perm:[1,0,3,2] row_mask:0xf bank_mask:0xf bound_ctrl:1
	s_nop 0
	v_add_f32_dpp v98, v137, v137 quad_perm:[1,0,3,2] row_mask:0xf bank_mask:0xf bound_ctrl:1
	v_cndmask_b32_e64 v99, v138, v98, s[16:17]
	v_bfe_u32 v7, v99, 16, 1
	v_add3_u32 v7, v99, v7, s3
	s_cmp_eq_u32 s8, 0
	s_cbranch_scc1 .Lsc_nost
	global_store_short_d16_hi v[8:9], v7, off
.Lsc_nost:
	v_add_f32_dpp v132, v130, v130 row_mirror row_mask:0xf bank_mask:0x3 bound_ctrl:1
	s_waitcnt lgkmcnt(6)
	v_pk_mul_f32 v[126:127], v[14:15], v[100:101]
	v_pk_mul_f32 v[128:129], v[14:15], v[64:65]
	v_pk_fma_f32 v[126:127], v[16:17], v[102:103], v[126:127]
	v_pk_fma_f32 v[128:129], v[16:17], v[66:67], v[128:129]
	v_add_f32_e32 v124, v126, v127
	v_pk_fma_f32 v[14:15], v[108:109], v[122:123], v[14:15] op_sel:[0,1,0]
	v_add_f32_e32 v130, v128, v129
	v_add_f32_dpp v124, v124, v124 quad_perm:[1,0,3,2] row_mask:0xf bank_mask:0xf bound_ctrl:1
	v_pk_fma_f32 v[16:17], v[110:111], v[122:123], v[16:17] op_sel:[0,1,0]
	ds_read_b128 v[36:39], v18 offset:1280
	v_add_f32_dpp v124, v124, v124 quad_perm:[2,3,0,1] row_mask:0xf bank_mask:0xf bound_ctrl:1
	ds_read_b128 v[44:47], v18 offset:25856
	ds_read_b128 v[40:43], v18 offset:9472
	v_add_f32_dpp v124, v124, v124 row_half_mirror row_mask:0xf bank_mask:0xf bound_ctrl:1
	ds_read_b128 v[48:51], v18 offset:34048
	v_lshl_add_u64 v[4:5], v[4:5], 1, v[12:13]
	v_add_f32_dpp v124, v124, v124 row_mirror row_mask:0xf bank_mask:0xf bound_ctrl:1
	v_pk_fma_f32 v[14:15], v[104:105], v[124:125], v[14:15] op_sel_hi:[1,0,1] neg_lo:[0,1,0] neg_hi:[0,1,0]
	v_pk_fma_f32 v[16:17], v[106:107], v[124:125], v[16:17] op_sel_hi:[1,0,1] neg_lo:[0,1,0] neg_hi:[0,1,0]
	v_pk_mul_f32 v[14:15], v[14:15], v[116:117]
	v_pk_mul_f32 v[16:17], v[16:17], v[118:119]
	v_add_f32_dpp v132, v131, v131 row_mirror row_mask:0xf bank_mask:0xc bound_ctrl:1
	s_waitcnt lgkmcnt(5)
	v_pk_mul_f32 v[126:127], v[14:15], v[20:21]
	v_pk_mul_f32 v[128:129], v[14:15], v[112:113]
	v_pk_fma_f32 v[126:127], v[16:17], v[22:23], v[126:127]
	v_pk_fma_f32 v[128:129], v[16:17], v[114:115], v[128:129]
	v_add_f32_e32 v124, v126, v127
	v_pk_fma_f32 v[14:15], v[28:29], v[120:121], v[14:15] op_sel_hi:[1,0,1]
	v_add_f32_e32 v131, v128, v129
	v_add_f32_dpp v124, v124, v124 quad_perm:[1,0,3,2] row_mask:0xf bank_mask:0xf bound_ctrl:1
	v_pk_fma_f32 v[16:17], v[30:31], v[120:121], v[16:17] op_sel_hi:[1,0,1]
	ds_read_b128 v[52:55], v18 offset:1536
	v_add_f32_dpp v124, v124, v124 quad_perm:[2,3,0,1] row_mask:0xf bank_mask:0xf bound_ctrl:1
	ds_read_b128 v[60:63], v18 offset:26112
	ds_read2_b32 v[122:123], v2 offset0:96 offset1:112
	v_add_f32_dpp v124, v124, v124 row_half_mirror row_mask:0xf bank_mask:0xf bound_ctrl:1
	ds_read_b128 v[56:59], v18 offset:9728
	ds_read_b128 v[64:67], v18 offset:34304
	v_add_f32_dpp v124, v124, v124 row_mirror row_mask:0xf bank_mask:0xf bound_ctrl:1
	v_pk_fma_f32 v[14:15], v[24:25], v[124:125], v[14:15] op_sel_hi:[1,0,1] neg_lo:[0,1,0] neg_hi:[0,1,0]
	v_pk_fma_f32 v[16:17], v[26:27], v[124:125], v[16:17] op_sel_hi:[1,0,1] neg_lo:[0,1,0] neg_hi:[0,1,0]
	v_add_f32_dpp v133, v130, v130 row_mirror row_mask:0xf bank_mask:0x3 bound_ctrl:1
	s_waitcnt lgkmcnt(6)
	v_pk_mul_f32 v[126:127], v[14:15], v[36:37]
	v_pk_mul_f32 v[128:129], v[14:15], v[32:33]
	v_pk_fma_f32 v[126:127], v[16:17], v[38:39], v[126:127]
	v_pk_fma_f32 v[128:129], v[16:17], v[34:35], v[128:129]
	v_add_f32_e32 v124, v126, v127
	v_pk_fma_f32 v[14:15], v[44:45], v[120:121], v[14:15] op_sel:[0,1,0]
	v_add_f32_e32 v130, v128, v129
	v_add_f32_dpp v124, v124, v124 quad_perm:[1,0,3,2] row_mask:0xf bank_mask:0xf bound_ctrl:1
	v_pk_fma_f32 v[16:17], v[46:47], v[120:121], v[16:17] op_sel:[0,1,0]
	ds_read_b128 v[100:103], v18 offset:1792
	v_add_f32_dpp v124, v124, v124 quad_perm:[2,3,0,1] row_mask:0xf bank_mask:0xf bound_ctrl:1
	ds_read_b128 v[108:111], v18 offset:26368
	ds_read_b128 v[116:119], v18 offset:18176
	v_add_f32_dpp v124, v124, v124 row_half_mirror row_mask:0xf bank_mask:0xf bound_ctrl:1
	ds_read_b128 v[104:107], v18 offset:9984
	ds_read_b128 v[112:115], v18 offset:34560
	v_add_f32_dpp v124, v124, v124 row_mirror row_mask:0xf bank_mask:0xf bound_ctrl:1
	v_pk_fma_f32 v[14:15], v[40:41], v[124:125], v[14:15] op_sel_hi:[1,0,1] neg_lo:[0,1,0] neg_hi:[0,1,0]
	v_pk_fma_f32 v[16:17], v[42:43], v[124:125], v[16:17] op_sel_hi:[1,0,1] neg_lo:[0,1,0] neg_hi:[0,1,0]
	v_add_f32_dpp v133, v131, v131 row_mirror row_mask:0xf bank_mask:0xc bound_ctrl:1
	v_add_f32_dpp v134, v132, v132 row_half_mirror row_mask:0xf bank_mask:0x5 bound_ctrl:1
	s_waitcnt lgkmcnt(6)
	v_pk_mul_f32 v[126:127], v[14:15], v[52:53]
	v_pk_mul_f32 v[128:129], v[14:15], v[48:49]
	v_pk_fma_f32 v[126:127], v[16:17], v[54:55], v[126:127]
	v_pk_fma_f32 v[128:129], v[16:17], v[50:51], v[128:129]
	v_add_f32_e32 v124, v126, v127
	v_pk_fma_f32 v[14:15], v[60:61], v[122:123], v[14:15] op_sel_hi:[1,0,1]
	v_add_f32_e32 v131, v128, v129
	v_add_f32_dpp v124, v124, v124 quad_perm:[1,0,3,2] row_mask:0xf bank_mask:0xf bound_ctrl:1
	v_pk_fma_f32 v[16:17], v[62:63], v[122:123], v[16:17] op_sel_hi:[1,0,1]
	ds_read_b128 v[20:23], v18 offset:2048
	v_add_f32_dpp v124, v124, v124 quad_perm:[2,3,0,1] row_mask:0xf bank_mask:0xf bound_ctrl:1
	ds_read_b128 v[28:31], v18 offset:26624
	ds_read2_b32 v[120:121], v2 offset0:128 offset1:144
	v_add_f32_dpp v124, v124, v124 row_half_mirror row_mask:0xf bank_mask:0xf bound_ctrl:1
	ds_read_b128 v[24:27], v18 offset:10240
	ds_read_b128 v[32:35], v18 offset:34816
	v_add_f32_dpp v124, v124, v124 row_mirror row_mask:0xf bank_mask:0xf bound_ctrl:1
	v_pk_fma_f32 v[14:15], v[56:57], v[124:125], v[14:15] op_sel_hi:[1,0,1] neg_lo:[0,1,0] neg_hi:[0,1,0]
	v_pk_fma_f32 v[16:17], v[58:59], v[124:125], v[16:17] op_sel_hi:[1,0,1] neg_lo:[0,1,0] neg_hi:[0,1,0]
	v_add_f32_dpp v134, v133, v133 row_half_mirror row_mask:0xf bank_mask:0xa bound_ctrl:1
	v_add_f32_dpp v132, v130, v130 row_mirror row_mask:0xf bank_mask:0x3 bound_ctrl:1
	s_waitcnt lgkmcnt(6)
	v_pk_mul_f32 v[126:127], v[14:15], v[100:101]
	v_pk_mul_f32 v[128:129], v[14:15], v[64:65]
	v_pk_fma_f32 v[126:127], v[16:17], v[102:103], v[126:127]
	v_pk_fma_f32 v[128:129], v[16:17], v[66:67], v[128:129]
	v_add_f32_e32 v124, v126, v127
	v_pk_fma_f32 v[14:15], v[108:109], v[122:123], v[14:15] op_sel:[0,1,0]
	v_add_f32_e32 v130, v128, v129
	v_add_f32_dpp v124, v124, v124 quad_perm:[1,0,3,2] row_mask:0xf bank_mask:0xf bound_ctrl:1
	v_pk_fma_f32 v[16:17], v[110:111], v[122:123], v[16:17] op_sel:[0,1,0]
	ds_read_b128 v[36:39], v18 offset:2304
	v_add_f32_dpp v124, v124, v124 quad_perm:[2,3,0,1] row_mask:0xf bank_mask:0xf bound_ctrl:1
	ds_read_b128 v[44:47], v18 offset:26880
	ds_read_b128 v[40:43], v18 offset:10496
	v_add_f32_dpp v124, v124, v124 row_half_mirror row_mask:0xf bank_mask:0xf bound_ctrl:1
	ds_read_b128 v[48:51], v18 offset:35072
	v_add_f32_dpp v132, v131, v131 row_mirror row_mask:0xf bank_mask:0xc bound_ctrl:1
	v_add_f32_dpp v124, v124, v124 row_mirror row_mask:0xf bank_mask:0xf bound_ctrl:1
	v_pk_fma_f32 v[14:15], v[104:105], v[124:125], v[14:15] op_sel_hi:[1,0,1] neg_lo:[0,1,0] neg_hi:[0,1,0]
	v_pk_fma_f32 v[16:17], v[106:107], v[124:125], v[16:17] op_sel_hi:[1,0,1] neg_lo:[0,1,0] neg_hi:[0,1,0]
	v_pk_mul_f32 v[14:15], v[14:15], v[116:117]
	v_pk_mul_f32 v[16:17], v[16:17], v[118:119]
	s_waitcnt lgkmcnt(5)
	v_pk_mul_f32 v[126:127], v[14:15], v[20:21]
	v_pk_mul_f32 v[128:129], v[14:15], v[112:113]
	v_pk_fma_f32 v[126:127], v[16:17], v[22:23], v[126:127]
	v_pk_fma_f32 v[128:129], v[16:17], v[114:115], v[128:129]
	v_add_f32_e32 v124, v126, v127
	v_pk_fma_f32 v[14:15], v[28:29], v[120:121], v[14:15] op_sel_hi:[1,0,1]
	v_add_f32_e32 v131, v128, v129
	v_add_f32_dpp v124, v124, v124 quad_perm:[1,0,3,2] row_mask:0xf bank_mask:0xf bound_ctrl:1
	v_pk_fma_f32 v[16:17], v[30:31], v[120:121], v[16:17] op_sel_hi:[1,0,1]
	ds_read_b128 v[52:55], v18 offset:2560
	v_add_f32_dpp v124, v124, v124 quad_perm:[2,3,0,1] row_mask:0xf bank_mask:0xf bound_ctrl:1
	ds_read_b128 v[60:63], v18 offset:27136
	ds_read2_b32 v[122:123], v2 offset0:160 offset1:176
	v_add_f32_dpp v124, v124, v124 row_half_mirror row_mask:0xf bank_mask:0xf bound_ctrl:1
	ds_read_b128 v[56:59], v18 offset:10752
	ds_read_b128 v[64:67], v18 offset:35328
	v_add_f32_dpp v124, v124, v124 row_mirror row_mask:0xf bank_mask:0xf bound_ctrl:1
	v_pk_fma_f32 v[14:15], v[24:25], v[124:125], v[14:15] op_sel_hi:[1,0,1] neg_lo:[0,1,0] neg_hi:[0,1,0]
	v_pk_fma_f32 v[16:17], v[26:27], v[124:125], v[16:17] op_sel_hi:[1,0,1] neg_lo:[0,1,0] neg_hi:[0,1,0]
	v_add_f32_dpp v133, v130, v130 row_mirror row_mask:0xf bank_mask:0x3 bound_ctrl:1
	s_waitcnt lgkmcnt(6)
	v_pk_mul_f32 v[126:127], v[14:15], v[36:37]
	v_pk_mul_f32 v[128:129], v[14:15], v[32:33]
	v_pk_fma_f32 v[126:127], v[16:17], v[38:39], v[126:127]
	v_pk_fma_f32 v[128:129], v[16:17], v[34:35], v[128:129]
	v_add_f32_e32 v124, v126, v127
	v_pk_fma_f32 v[14:15], v[44:45], v[120:121], v[14:15] op_sel:[0,1,0]
	v_add_f32_e32 v130, v128, v129
	v_add_f32_dpp v124, v124, v124 quad_perm:[1,0,3,2] row_mask:0xf bank_mask:0xf bound_ctrl:1
	v_pk_fma_f32 v[16:17], v[46:47], v[120:121], v[16:17] op_sel:[0,1,0]
	ds_read_b128 v[100:103], v18 offset:2816
	v_add_f32_dpp v124, v124, v124 quad_perm:[2,3,0,1] row_mask:0xf bank_mask:0xf bound_ctrl:1
	ds_read_b128 v[108:111], v18 offset:27392
	ds_read_b128 v[116:119], v18 offset:19200
	v_add_f32_dpp v124, v124, v124 row_half_mirror row_mask:0xf bank_mask:0xf bound_ctrl:1
	ds_read_b128 v[104:107], v18 offset:11008
	ds_read_b128 v[112:115], v18 offset:35584
	v_add_f32_dpp v124, v124, v124 row_mirror row_mask:0xf bank_mask:0xf bound_ctrl:1
	v_pk_fma_f32 v[14:15], v[40:41], v[124:125], v[14:15] op_sel_hi:[1,0,1] neg_lo:[0,1,0] neg_hi:[0,1,0]
	v_pk_fma_f32 v[16:17], v[42:43], v[124:125], v[16:17] op_sel_hi:[1,0,1] neg_lo:[0,1,0] neg_hi:[0,1,0]
	v_add_f32_dpp v133, v131, v131 row_mirror row_mask:0xf bank_mask:0xc bound_ctrl:1
	v_add_f32_dpp v135, v132, v132 row_half_mirror row_mask:0xf bank_mask:0x5 bound_ctrl:1
	s_waitcnt lgkmcnt(6)
	v_pk_mul_f32 v[126:127], v[14:15], v[52:53]
	v_pk_mul_f32 v[128:129], v[14:15], v[48:49]
	v_pk_fma_f32 v[126:127], v[16:17], v[54:55], v[126:127]
	v_pk_fma_f32 v[128:129], v[16:17], v[50:51], v[128:129]
	v_add_f32_e32 v124, v126, v127
	v_pk_fma_f32 v[14:15], v[60:61], v[122:123], v[14:15] op_sel_hi:[1,0,1]
	v_add_f32_e32 v131, v128, v129
	v_add_f32_dpp v124, v124, v124 quad_perm:[1,0,3,2] row_mask:0xf bank_mask:0xf bound_ctrl:1
	v_pk_fma_f32 v[16:17], v[62:63], v[122:123], v[16:17] op_sel_hi:[1,0,1]
	ds_read_b128 v[20:23], v18 offset:3072
	v_add_f32_dpp v124, v124, v124 quad_perm:[2,3,0,1] row_mask:0xf bank_mask:0xf bound_ctrl:1
	ds_read_b128 v[28:31], v18 offset:27648
	ds_read2_b32 v[120:121], v2 offset0:192 offset1:208
	v_add_f32_dpp v124, v124, v124 row_half_mirror row_mask:0xf bank_mask:0xf bound_ctrl:1
	ds_read_b128 v[24:27], v18 offset:11264
	ds_read_b128 v[32:35], v18 offset:35840
	v_add_f32_dpp v124, v124, v124 row_mirror row_mask:0xf bank_mask:0xf bound_ctrl:1
	v_pk_fma_f32 v[14:15], v[56:57], v[124:125], v[14:15] op_sel_hi:[1,0,1] neg_lo:[0,1,0] neg_hi:[0,1,0]
	v_pk_fma_f32 v[16:17], v[58:59], v[124:125], v[16:17] op_sel_hi:[1,0,1] neg_lo:[0,1,0] neg_hi:[0,1,0]
	v_add_f32_dpp v135, v133, v133 row_half_mirror row_mask:0xf bank_mask:0xa bound_ctrl:1
	v_add_f32_dpp v138, v134, v134 quad_perm:[2,3,0,1] row_mask:0xf bank_mask:0xf bound_ctrl:1
	s_nop 0
	v_add_f32_dpp v98, v135, v135 quad_perm:[2,3,0,1] row_mask:0xf bank_mask:0xf bound_ctrl:1
	v_cndmask_b32_e64 v136, v138, v98, s[14:15]
	v_add_f32_dpp v132, v130, v130 row_mirror row_mask:0xf bank_mask:0x3 bound_ctrl:1
	s_waitcnt lgkmcnt(6)
	v_pk_mul_f32 v[126:127], v[14:15], v[100:101]
	v_pk_mul_f32 v[128:129], v[14:15], v[64:65]
	v_pk_fma_f32 v[126:127], v[16:17], v[102:103], v[126:127]
	v_pk_fma_f32 v[128:129], v[16:17], v[66:67], v[128:129]
	v_add_f32_e32 v124, v126, v127
	v_pk_fma_f32 v[14:15], v[108:109], v[122:123], v[14:15] op_sel:[0,1,0]
	v_add_f32_e32 v130, v128, v129
	v_add_f32_dpp v124, v124, v124 quad_perm:[1,0,3,2] row_mask:0xf bank_mask:0xf bound_ctrl:1
	v_pk_fma_f32 v[16:17], v[110:111], v[122:123], v[16:17] op_sel:[0,1,0]
	ds_read_b128 v[36:39], v18 offset:3328
	v_add_f32_dpp v124, v124, v124 quad_perm:[2,3,0,1] row_mask:0xf bank_mask:0xf bound_ctrl:1
	ds_read_b128 v[44:47], v18 offset:27904
	ds_read_b128 v[40:43], v18 offset:11520
	v_add_f32_dpp v124, v124, v124 row_half_mirror row_mask:0xf bank_mask:0xf bound_ctrl:1
	ds_read_b128 v[48:51], v18 offset:36096
	v_add_f32_dpp v132, v131, v131 row_mirror row_mask:0xf bank_mask:0xc bound_ctrl:1
	v_add_f32_dpp v124, v124, v124 row_mirror row_mask:0xf bank_mask:0xf bound_ctrl:1
	v_pk_fma_f32 v[14:15], v[104:105], v[124:125], v[14:15] op_sel_hi:[1,0,1] neg_lo:[0,1,0] neg_hi:[0,1,0]
	v_pk_fma_f32 v[16:17], v[106:107], v[124:125], v[16:17] op_sel_hi:[1,0,1] neg_lo:[0,1,0] neg_hi:[0,1,0]
	v_pk_mul_f32 v[14:15], v[14:15], v[116:117]
	v_pk_mul_f32 v[16:17], v[16:17], v[118:119]
	s_waitcnt lgkmcnt(5)
	v_pk_mul_f32 v[126:127], v[14:15], v[20:21]
	v_pk_mul_f32 v[128:129], v[14:15], v[112:113]
	v_pk_fma_f32 v[126:127], v[16:17], v[22:23], v[126:127]
	v_pk_fma_f32 v[128:129], v[16:17], v[114:115], v[128:129]
	v_add_f32_e32 v124, v126, v127
	v_pk_fma_f32 v[14:15], v[28:29], v[120:121], v[14:15] op_sel_hi:[1,0,1]
	v_add_f32_e32 v131, v128, v129
	v_add_f32_dpp v124, v124, v124 quad_perm:[1,0,3,2] row_mask:0xf bank_mask:0xf bound_ctrl:1
	v_pk_fma_f32 v[16:17], v[30:31], v[120:121], v[16:17] op_sel_hi:[1,0,1]
	ds_read_b128 v[52:55], v18 offset:3584
	v_add_f32_dpp v124, v124, v124 quad_perm:[2,3,0,1] row_mask:0xf bank_mask:0xf bound_ctrl:1
	ds_read_b128 v[60:63], v18 offset:28160
	ds_read2_b32 v[122:123], v2 offset0:224 offset1:240
	v_add_f32_dpp v124, v124, v124 row_half_mirror row_mask:0xf bank_mask:0xf bound_ctrl:1
	ds_read_b128 v[56:59], v18 offset:11776
	ds_read_b128 v[64:67], v18 offset:36352
	v_add_f32_dpp v124, v124, v124 row_mirror row_mask:0xf bank_mask:0xf bound_ctrl:1
	v_pk_fma_f32 v[14:15], v[24:25], v[124:125], v[14:15] op_sel_hi:[1,0,1] neg_lo:[0,1,0] neg_hi:[0,1,0]
	v_pk_fma_f32 v[16:17], v[26:27], v[124:125], v[16:17] op_sel_hi:[1,0,1] neg_lo:[0,1,0] neg_hi:[0,1,0]
	v_mul_hi_i32_i24_e32 v9, s44, v94
	v_mul_i32_i24_e32 v8, s44, v94
	v_add_f32_dpp v133, v130, v130 row_mirror row_mask:0xf bank_mask:0x3 bound_ctrl:1
	s_waitcnt lgkmcnt(6)
	v_pk_mul_f32 v[126:127], v[14:15], v[36:37]
	v_pk_mul_f32 v[128:129], v[14:15], v[32:33]
	v_pk_fma_f32 v[126:127], v[16:17], v[38:39], v[126:127]
	v_pk_fma_f32 v[128:129], v[16:17], v[34:35], v[128:129]
	v_add_f32_e32 v124, v126, v127
	v_pk_fma_f32 v[14:15], v[44:45], v[120:121], v[14:15] op_sel:[0,1,0]
	v_add_f32_e32 v130, v128, v129
	v_add_f32_dpp v124, v124, v124 quad_perm:[1,0,3,2] row_mask:0xf bank_mask:0xf bound_ctrl:1
	v_pk_fma_f32 v[16:17], v[46:47], v[120:121], v[16:17] op_sel:[0,1,0]
	ds_read_b128 v[100:103], v18 offset:3840
	v_add_f32_dpp v124, v124, v124 quad_perm:[2,3,0,1] row_mask:0xf bank_mask:0xf bound_ctrl:1
	ds_read_b128 v[108:111], v18 offset:28416
	ds_read_b128 v[116:119], v18 offset:20224
	v_add_f32_dpp v124, v124, v124 row_half_mirror row_mask:0xf bank_mask:0xf bound_ctrl:1
	ds_read_b128 v[104:107], v18 offset:12032
	ds_read_b128 v[112:115], v18 offset:36608
	v_add_f32_dpp v124, v124, v124 row_mirror row_mask:0xf bank_mask:0xf bound_ctrl:1
	v_pk_fma_f32 v[14:15], v[40:41], v[124:125], v[14:15] op_sel_hi:[1,0,1] neg_lo:[0,1,0] neg_hi:[0,1,0]
	v_pk_fma_f32 v[16:17], v[42:43], v[124:125], v[16:17] op_sel_hi:[1,0,1] neg_lo:[0,1,0] neg_hi:[0,1,0]
	v_lshl_add_u64 v[8:9], v[8:9], 1, v[12:13]
	v_add_f32_dpp v133, v131, v131 row_mirror row_mask:0xf bank_mask:0xc bound_ctrl:1
	v_add_f32_dpp v134, v132, v132 row_half_mirror row_mask:0xf bank_mask:0x5 bound_ctrl:1
	s_waitcnt lgkmcnt(6)
	v_pk_mul_f32 v[126:127], v[14:15], v[52:53]
	v_pk_mul_f32 v[128:129], v[14:15], v[48:49]
	v_pk_fma_f32 v[126:127], v[16:17], v[54:55], v[126:127]
	v_pk_fma_f32 v[128:129], v[16:17], v[50:51], v[128:129]
	v_add_f32_e32 v124, v126, v127
	v_pk_fma_f32 v[14:15], v[60:61], v[122:123], v[14:15] op_sel_hi:[1,0,1]
	v_add_f32_e32 v131, v128, v129
	v_add_f32_dpp v124, v124, v124 quad_perm:[1,0,3,2] row_mask:0xf bank_mask:0xf bound_ctrl:1
	v_pk_fma_f32 v[16:17], v[62:63], v[122:123], v[16:17] op_sel_hi:[1,0,1]
	ds_read_b128 v[20:23], v18 offset:4096
	v_add_f32_dpp v124, v124, v124 quad_perm:[2,3,0,1] row_mask:0xf bank_mask:0xf bound_ctrl:1
	ds_read_b128 v[28:31], v18 offset:28672
	ds_read2_b32 v[120:121], v3 offset1:16
	v_add_f32_dpp v124, v124, v124 row_half_mirror row_mask:0xf bank_mask:0xf bound_ctrl:1
	ds_read_b128 v[24:27], v18 offset:12288
	ds_read_b128 v[32:35], v18 offset:36864
	v_add_f32_dpp v124, v124, v124 row_mirror row_mask:0xf bank_mask:0xf bound_ctrl:1
	v_pk_fma_f32 v[14:15], v[56:57], v[124:125], v[14:15] op_sel_hi:[1,0,1] neg_lo:[0,1,0] neg_hi:[0,1,0]
	v_pk_fma_f32 v[16:17], v[58:59], v[124:125], v[16:17] op_sel_hi:[1,0,1] neg_lo:[0,1,0] neg_hi:[0,1,0]
	v_add_f32_dpp v134, v133, v133 row_half_mirror row_mask:0xf bank_mask:0xa bound_ctrl:1
	v_add_f32_dpp v132, v130, v130 row_mirror row_mask:0xf bank_mask:0x3 bound_ctrl:1
	s_waitcnt lgkmcnt(6)
	v_pk_mul_f32 v[126:127], v[14:15], v[100:101]
	v_pk_mul_f32 v[128:129], v[14:15], v[64:65]
	v_pk_fma_f32 v[126:127], v[16:17], v[102:103], v[126:127]
	v_pk_fma_f32 v[128:129], v[16:17], v[66:67], v[128:129]
	v_add_f32_e32 v124, v126, v127
	v_pk_fma_f32 v[14:15], v[108:109], v[122:123], v[14:15] op_sel:[0,1,0]
	v_add_f32_e32 v130, v128, v129
	v_add_f32_dpp v124, v124, v124 quad_perm:[1,0,3,2] row_mask:0xf bank_mask:0xf bound_ctrl:1
	v_pk_fma_f32 v[16:17], v[110:111], v[122:123], v[16:17] op_sel:[0,1,0]
	ds_read_b128 v[36:39], v18 offset:4352
	v_add_f32_dpp v124, v124, v124 quad_perm:[2,3,0,1] row_mask:0xf bank_mask:0xf bound_ctrl:1
	ds_read_b128 v[44:47], v18 offset:28928
	ds_read_b128 v[40:43], v18 offset:12544
	v_add_f32_dpp v124, v124, v124 row_half_mirror row_mask:0xf bank_mask:0xf bound_ctrl:1
	ds_read_b128 v[48:51], v18 offset:37120
	v_add_f32_dpp v132, v131, v131 row_mirror row_mask:0xf bank_mask:0xc bound_ctrl:1
	v_add_f32_dpp v124, v124, v124 row_mirror row_mask:0xf bank_mask:0xf bound_ctrl:1
	v_pk_fma_f32 v[14:15], v[104:105], v[124:125], v[14:15] op_sel_hi:[1,0,1] neg_lo:[0,1,0] neg_hi:[0,1,0]
	v_pk_fma_f32 v[16:17], v[106:107], v[124:125], v[16:17] op_sel_hi:[1,0,1] neg_lo:[0,1,0] neg_hi:[0,1,0]
	v_pk_mul_f32 v[14:15], v[14:15], v[116:117]
	v_pk_mul_f32 v[16:17], v[16:17], v[118:119]
	s_waitcnt lgkmcnt(5)
	v_pk_mul_f32 v[126:127], v[14:15], v[20:21]
	v_pk_mul_f32 v[128:129], v[14:15], v[112:113]
	v_pk_fma_f32 v[126:127], v[16:17], v[22:23], v[126:127]
	v_pk_fma_f32 v[128:129], v[16:17], v[114:115], v[128:129]
	v_add_f32_e32 v124, v126, v127
	v_pk_fma_f32 v[14:15], v[28:29], v[120:121], v[14:15] op_sel_hi:[1,0,1]
	v_add_f32_e32 v131, v128, v129
	v_add_f32_dpp v124, v124, v124 quad_perm:[1,0,3,2] row_mask:0xf bank_mask:0xf bound_ctrl:1
	v_pk_fma_f32 v[16:17], v[30:31], v[120:121], v[16:17] op_sel_hi:[1,0,1]
	ds_read_b128 v[52:55], v18 offset:4608
	v_add_f32_dpp v124, v124, v124 quad_perm:[2,3,0,1] row_mask:0xf bank_mask:0xf bound_ctrl:1
	ds_read_b128 v[60:63], v18 offset:29184
	ds_read2_b32 v[122:123], v3 offset0:32 offset1:48
	v_add_f32_dpp v124, v124, v124 row_half_mirror row_mask:0xf bank_mask:0xf bound_ctrl:1
	ds_read_b128 v[56:59], v18 offset:12800
	ds_read_b128 v[64:67], v18 offset:37376
	v_add_f32_dpp v124, v124, v124 row_mirror row_mask:0xf bank_mask:0xf bound_ctrl:1
	v_pk_fma_f32 v[14:15], v[24:25], v[124:125], v[14:15] op_sel_hi:[1,0,1] neg_lo:[0,1,0] neg_hi:[0,1,0]
	v_pk_fma_f32 v[16:17], v[26:27], v[124:125], v[16:17] op_sel_hi:[1,0,1] neg_lo:[0,1,0] neg_hi:[0,1,0]
	v_add_f32_dpp v133, v130, v130 row_mirror row_mask:0xf bank_mask:0x3 bound_ctrl:1
	s_waitcnt lgkmcnt(6)
	v_pk_mul_f32 v[126:127], v[14:15], v[36:37]
	v_pk_mul_f32 v[128:129], v[14:15], v[32:33]
	v_pk_fma_f32 v[126:127], v[16:17], v[38:39], v[126:127]
	v_pk_fma_f32 v[128:129], v[16:17], v[34:35], v[128:129]
	v_add_f32_e32 v124, v126, v127
	v_pk_fma_f32 v[14:15], v[44:45], v[120:121], v[14:15] op_sel:[0,1,0]
	v_add_f32_e32 v130, v128, v129
	v_add_f32_dpp v124, v124, v124 quad_perm:[1,0,3,2] row_mask:0xf bank_mask:0xf bound_ctrl:1
	v_pk_fma_f32 v[16:17], v[46:47], v[120:121], v[16:17] op_sel:[0,1,0]
	ds_read_b128 v[100:103], v18 offset:4864
	v_add_f32_dpp v124, v124, v124 quad_perm:[2,3,0,1] row_mask:0xf bank_mask:0xf bound_ctrl:1
	ds_read_b128 v[108:111], v18 offset:29440
	ds_read_b128 v[116:119], v18 offset:21248
	v_add_f32_dpp v124, v124, v124 row_half_mirror row_mask:0xf bank_mask:0xf bound_ctrl:1
	ds_read_b128 v[104:107], v18 offset:13056
	ds_read_b128 v[112:115], v18 offset:37632
	v_add_f32_dpp v124, v124, v124 row_mirror row_mask:0xf bank_mask:0xf bound_ctrl:1
	v_pk_fma_f32 v[14:15], v[40:41], v[124:125], v[14:15] op_sel_hi:[1,0,1] neg_lo:[0,1,0] neg_hi:[0,1,0]
	v_pk_fma_f32 v[16:17], v[42:43], v[124:125], v[16:17] op_sel_hi:[1,0,1] neg_lo:[0,1,0] neg_hi:[0,1,0]
	v_add_f32_dpp v133, v131, v131 row_mirror row_mask:0xf bank_mask:0xc bound_ctrl:1
	v_add_f32_dpp v135, v132, v132 row_half_mirror row_mask:0xf bank_mask:0x5 bound_ctrl:1
	s_waitcnt lgkmcnt(6)
	v_pk_mul_f32 v[126:127], v[14:15], v[52:53]
	v_pk_mul_f32 v[128:129], v[14:15], v[48:49]
	v_pk_fma_f32 v[126:127], v[16:17], v[54:55], v[126:127]
	v_pk_fma_f32 v[128:129], v[16:17], v[50:51], v[128:129]
	v_add_f32_e32 v124, v126, v127
	v_pk_fma_f32 v[14:15], v[60:61], v[122:123], v[14:15] op_sel_hi:[1,0,1]
	v_add_f32_e32 v131, v128, v129
	v_add_f32_dpp v124, v124, v124 quad_perm:[1,0,3,2] row_mask:0xf bank_mask:0xf bound_ctrl:1
	v_pk_fma_f32 v[16:17], v[62:63], v[122:123], v[16:17] op_sel_hi:[1,0,1]
	ds_read_b128 v[20:23], v18 offset:5120
	v_add_f32_dpp v124, v124, v124 quad_perm:[2,3,0,1] row_mask:0xf bank_mask:0xf bound_ctrl:1
	ds_read_b128 v[28:31], v18 offset:29696
	ds_read2_b32 v[120:121], v3 offset0:64 offset1:80
	v_add_f32_dpp v124, v124, v124 row_half_mirror row_mask:0xf bank_mask:0xf bound_ctrl:1
	ds_read_b128 v[24:27], v18 offset:13312
	ds_read_b128 v[32:35], v18 offset:37888
	v_add_f32_dpp v124, v124, v124 row_mirror row_mask:0xf bank_mask:0xf bound_ctrl:1
	v_pk_fma_f32 v[14:15], v[56:57], v[124:125], v[14:15] op_sel_hi:[1,0,1] neg_lo:[0,1,0] neg_hi:[0,1,0]
	v_pk_fma_f32 v[16:17], v[58:59], v[124:125], v[16:17] op_sel_hi:[1,0,1] neg_lo:[0,1,0] neg_hi:[0,1,0]
	v_add_f32_dpp v135, v133, v133 row_half_mirror row_mask:0xf bank_mask:0xa bound_ctrl:1
	v_add_f32_dpp v138, v134, v134 quad_perm:[2,3,0,1] row_mask:0xf bank_mask:0xf bound_ctrl:1
	s_nop 0
	v_add_f32_dpp v98, v135, v135 quad_perm:[2,3,0,1] row_mask:0xf bank_mask:0xf bound_ctrl:1
	v_cndmask_b32_e64 v137, v138, v98, s[14:15]
	v_add_f32_dpp v138, v136, v136 quad_perm:[1,0,3,2] row_mask:0xf bank_mask:0xf bound_ctrl:1
	s_nop 0
	v_add_f32_dpp v98, v137, v137 quad_perm:[1,0,3,2] row_mask:0xf bank_mask:0xf bound_ctrl:1
	v_cndmask_b32_e64 v99, v138, v98, s[16:17]
	v_bfe_u32 v6, v99, 16, 1
	v_add3_u32 v6, v99, v6, s3
	global_store_short_d16_hi v[4:5], v6, off
	v_add_f32_dpp v132, v130, v130 row_mirror row_mask:0xf bank_mask:0x3 bound_ctrl:1
	s_waitcnt lgkmcnt(6)
	v_pk_mul_f32 v[126:127], v[14:15], v[100:101]
	v_pk_mul_f32 v[128:129], v[14:15], v[64:65]
	v_pk_fma_f32 v[126:127], v[16:17], v[102:103], v[126:127]
	v_pk_fma_f32 v[128:129], v[16:17], v[66:67], v[128:129]
	v_add_f32_e32 v124, v126, v127
	v_pk_fma_f32 v[14:15], v[108:109], v[122:123], v[14:15] op_sel:[0,1,0]
	v_add_f32_e32 v130, v128, v129
	v_add_f32_dpp v124, v124, v124 quad_perm:[1,0,3,2] row_mask:0xf bank_mask:0xf bound_ctrl:1
	v_pk_fma_f32 v[16:17], v[110:111], v[122:123], v[16:17] op_sel:[0,1,0]
	ds_read_b128 v[36:39], v18 offset:5376
	v_add_f32_dpp v124, v124, v124 quad_perm:[2,3,0,1] row_mask:0xf bank_mask:0xf bound_ctrl:1
	ds_read_b128 v[44:47], v18 offset:29952
	ds_read_b128 v[40:43], v18 offset:13568
	v_add_f32_dpp v124, v124, v124 row_half_mirror row_mask:0xf bank_mask:0xf bound_ctrl:1
	ds_read_b128 v[48:51], v18 offset:38144
	v_add_f32_dpp v132, v131, v131 row_mirror row_mask:0xf bank_mask:0xc bound_ctrl:1
	v_add_f32_dpp v124, v124, v124 row_mirror row_mask:0xf bank_mask:0xf bound_ctrl:1
	v_pk_fma_f32 v[14:15], v[104:105], v[124:125], v[14:15] op_sel_hi:[1,0,1] neg_lo:[0,1,0] neg_hi:[0,1,0]
	v_pk_fma_f32 v[16:17], v[106:107], v[124:125], v[16:17] op_sel_hi:[1,0,1] neg_lo:[0,1,0] neg_hi:[0,1,0]
	v_pk_mul_f32 v[14:15], v[14:15], v[116:117]
	v_pk_mul_f32 v[16:17], v[16:17], v[118:119]
	s_waitcnt lgkmcnt(5)
	v_pk_mul_f32 v[126:127], v[14:15], v[20:21]
	v_pk_mul_f32 v[128:129], v[14:15], v[112:113]
	v_pk_fma_f32 v[126:127], v[16:17], v[22:23], v[126:127]
	v_pk_fma_f32 v[128:129], v[16:17], v[114:115], v[128:129]
	v_add_f32_e32 v124, v126, v127
	v_pk_fma_f32 v[14:15], v[28:29], v[120:121], v[14:15] op_sel_hi:[1,0,1]
	v_add_f32_e32 v131, v128, v129
	v_add_f32_dpp v124, v124, v124 quad_perm:[1,0,3,2] row_mask:0xf bank_mask:0xf bound_ctrl:1
	v_pk_fma_f32 v[16:17], v[30:31], v[120:121], v[16:17] op_sel_hi:[1,0,1]
	ds_read_b128 v[52:55], v18 offset:5632
	v_add_f32_dpp v124, v124, v124 quad_perm:[2,3,0,1] row_mask:0xf bank_mask:0xf bound_ctrl:1
	ds_read_b128 v[60:63], v18 offset:30208
	ds_read2_b32 v[122:123], v3 offset0:96 offset1:112
	v_add_f32_dpp v124, v124, v124 row_half_mirror row_mask:0xf bank_mask:0xf bound_ctrl:1
	ds_read_b128 v[56:59], v18 offset:13824
	ds_read_b128 v[64:67], v18 offset:38400
	v_add_f32_dpp v124, v124, v124 row_mirror row_mask:0xf bank_mask:0xf bound_ctrl:1
	v_pk_fma_f32 v[14:15], v[24:25], v[124:125], v[14:15] op_sel_hi:[1,0,1] neg_lo:[0,1,0] neg_hi:[0,1,0]
	v_pk_fma_f32 v[16:17], v[26:27], v[124:125], v[16:17] op_sel_hi:[1,0,1] neg_lo:[0,1,0] neg_hi:[0,1,0]
	v_add_f32_dpp v133, v130, v130 row_mirror row_mask:0xf bank_mask:0x3 bound_ctrl:1
	s_waitcnt lgkmcnt(6)
	v_pk_mul_f32 v[126:127], v[14:15], v[36:37]
	v_pk_mul_f32 v[128:129], v[14:15], v[32:33]
	v_pk_fma_f32 v[126:127], v[16:17], v[38:39], v[126:127]
	v_pk_fma_f32 v[128:129], v[16:17], v[34:35], v[128:129]
	v_add_f32_e32 v124, v126, v127
	v_pk_fma_f32 v[14:15], v[44:45], v[120:121], v[14:15] op_sel:[0,1,0]
	v_add_f32_e32 v130, v128, v129
	v_add_f32_dpp v124, v124, v124 quad_perm:[1,0,3,2] row_mask:0xf bank_mask:0xf bound_ctrl:1
	v_pk_fma_f32 v[16:17], v[46:47], v[120:121], v[16:17] op_sel:[0,1,0]
	ds_read_b128 v[100:103], v18 offset:5888
	v_add_f32_dpp v124, v124, v124 quad_perm:[2,3,0,1] row_mask:0xf bank_mask:0xf bound_ctrl:1
	ds_read_b128 v[108:111], v18 offset:30464
	ds_read_b128 v[116:119], v18 offset:22272
	v_add_f32_dpp v124, v124, v124 row_half_mirror row_mask:0xf bank_mask:0xf bound_ctrl:1
	ds_read_b128 v[104:107], v18 offset:14080
	ds_read_b128 v[112:115], v18 offset:38656
	v_add_f32_dpp v124, v124, v124 row_mirror row_mask:0xf bank_mask:0xf bound_ctrl:1
	v_pk_fma_f32 v[14:15], v[40:41], v[124:125], v[14:15] op_sel_hi:[1,0,1] neg_lo:[0,1,0] neg_hi:[0,1,0]
	v_pk_fma_f32 v[16:17], v[42:43], v[124:125], v[16:17] op_sel_hi:[1,0,1] neg_lo:[0,1,0] neg_hi:[0,1,0]
	v_add_f32_dpp v133, v131, v131 row_mirror row_mask:0xf bank_mask:0xc bound_ctrl:1
	v_add_f32_dpp v134, v132, v132 row_half_mirror row_mask:0xf bank_mask:0x5 bound_ctrl:1
	s_waitcnt lgkmcnt(6)
	v_pk_mul_f32 v[126:127], v[14:15], v[52:53]
	v_pk_mul_f32 v[128:129], v[14:15], v[48:49]
	v_pk_fma_f32 v[126:127], v[16:17], v[54:55], v[126:127]
	v_pk_fma_f32 v[128:129], v[16:17], v[50:51], v[128:129]
	v_add_f32_e32 v124, v126, v127
	v_pk_fma_f32 v[14:15], v[60:61], v[122:123], v[14:15] op_sel_hi:[1,0,1]
	v_add_f32_e32 v131, v128, v129
	v_add_f32_dpp v124, v124, v124 quad_perm:[1,0,3,2] row_mask:0xf bank_mask:0xf bound_ctrl:1
	v_pk_fma_f32 v[16:17], v[62:63], v[122:123], v[16:17] op_sel_hi:[1,0,1]
	ds_read_b128 v[20:23], v18 offset:6144
	v_add_f32_dpp v124, v124, v124 quad_perm:[2,3,0,1] row_mask:0xf bank_mask:0xf bound_ctrl:1
	ds_read_b128 v[28:31], v18 offset:30720
	ds_read2_b32 v[120:121], v3 offset0:128 offset1:144
	v_add_f32_dpp v124, v124, v124 row_half_mirror row_mask:0xf bank_mask:0xf bound_ctrl:1
	ds_read_b128 v[24:27], v18 offset:14336
	ds_read_b128 v[32:35], v18 offset:38912
	v_add_f32_dpp v124, v124, v124 row_mirror row_mask:0xf bank_mask:0xf bound_ctrl:1
	v_pk_fma_f32 v[14:15], v[56:57], v[124:125], v[14:15] op_sel_hi:[1,0,1] neg_lo:[0,1,0] neg_hi:[0,1,0]
	v_pk_fma_f32 v[16:17], v[58:59], v[124:125], v[16:17] op_sel_hi:[1,0,1] neg_lo:[0,1,0] neg_hi:[0,1,0]
	v_add_f32_dpp v134, v133, v133 row_half_mirror row_mask:0xf bank_mask:0xa bound_ctrl:1
	v_add_f32_dpp v132, v130, v130 row_mirror row_mask:0xf bank_mask:0x3 bound_ctrl:1
	s_waitcnt lgkmcnt(6)
	v_pk_mul_f32 v[126:127], v[14:15], v[100:101]
	v_pk_mul_f32 v[128:129], v[14:15], v[64:65]
	v_pk_fma_f32 v[126:127], v[16:17], v[102:103], v[126:127]
	v_pk_fma_f32 v[128:129], v[16:17], v[66:67], v[128:129]
	v_add_f32_e32 v124, v126, v127
	v_pk_fma_f32 v[14:15], v[108:109], v[122:123], v[14:15] op_sel:[0,1,0]
	v_add_f32_e32 v130, v128, v129
	v_add_f32_dpp v124, v124, v124 quad_perm:[1,0,3,2] row_mask:0xf bank_mask:0xf bound_ctrl:1
	v_pk_fma_f32 v[16:17], v[110:111], v[122:123], v[16:17] op_sel:[0,1,0]
	ds_read_b128 v[36:39], v18 offset:6400
	v_add_f32_dpp v124, v124, v124 quad_perm:[2,3,0,1] row_mask:0xf bank_mask:0xf bound_ctrl:1
	ds_read_b128 v[44:47], v18 offset:30976
	ds_read_b128 v[40:43], v18 offset:14592
	v_add_f32_dpp v124, v124, v124 row_half_mirror row_mask:0xf bank_mask:0xf bound_ctrl:1
	ds_read_b128 v[48:51], v18 offset:39168
	v_add_f32_dpp v132, v131, v131 row_mirror row_mask:0xf bank_mask:0xc bound_ctrl:1
	v_add_f32_dpp v124, v124, v124 row_mirror row_mask:0xf bank_mask:0xf bound_ctrl:1
	v_pk_fma_f32 v[14:15], v[104:105], v[124:125], v[14:15] op_sel_hi:[1,0,1] neg_lo:[0,1,0] neg_hi:[0,1,0]
	v_pk_fma_f32 v[16:17], v[106:107], v[124:125], v[16:17] op_sel_hi:[1,0,1] neg_lo:[0,1,0] neg_hi:[0,1,0]
	v_pk_mul_f32 v[14:15], v[14:15], v[116:117]
	v_pk_mul_f32 v[16:17], v[16:17], v[118:119]
	s_waitcnt lgkmcnt(5)
	v_pk_mul_f32 v[126:127], v[14:15], v[20:21]
	v_pk_mul_f32 v[128:129], v[14:15], v[112:113]
	v_pk_fma_f32 v[126:127], v[16:17], v[22:23], v[126:127]
	v_pk_fma_f32 v[128:129], v[16:17], v[114:115], v[128:129]
	v_add_f32_e32 v124, v126, v127
	v_pk_fma_f32 v[14:15], v[28:29], v[120:121], v[14:15] op_sel_hi:[1,0,1]
	v_add_f32_e32 v131, v128, v129
	v_add_f32_dpp v124, v124, v124 quad_perm:[1,0,3,2] row_mask:0xf bank_mask:0xf bound_ctrl:1
	v_pk_fma_f32 v[16:17], v[30:31], v[120:121], v[16:17] op_sel_hi:[1,0,1]
	ds_read_b128 v[52:55], v18 offset:6656
	v_add_f32_dpp v124, v124, v124 quad_perm:[2,3,0,1] row_mask:0xf bank_mask:0xf bound_ctrl:1
	ds_read_b128 v[60:63], v18 offset:31232
	ds_read2_b32 v[122:123], v3 offset0:160 offset1:176
	v_add_f32_dpp v124, v124, v124 row_half_mirror row_mask:0xf bank_mask:0xf bound_ctrl:1
	ds_read_b128 v[56:59], v18 offset:14848
	ds_read_b128 v[64:67], v18 offset:39424
	v_add_f32_dpp v124, v124, v124 row_mirror row_mask:0xf bank_mask:0xf bound_ctrl:1
	v_pk_fma_f32 v[14:15], v[24:25], v[124:125], v[14:15] op_sel_hi:[1,0,1] neg_lo:[0,1,0] neg_hi:[0,1,0]
	v_pk_fma_f32 v[16:17], v[26:27], v[124:125], v[16:17] op_sel_hi:[1,0,1] neg_lo:[0,1,0] neg_hi:[0,1,0]
	v_add_f32_dpp v133, v130, v130 row_mirror row_mask:0xf bank_mask:0x3 bound_ctrl:1
	s_waitcnt lgkmcnt(6)
	v_pk_mul_f32 v[126:127], v[14:15], v[36:37]
	v_pk_mul_f32 v[128:129], v[14:15], v[32:33]
	v_pk_fma_f32 v[126:127], v[16:17], v[38:39], v[126:127]
	v_pk_fma_f32 v[128:129], v[16:17], v[34:35], v[128:129]
	v_add_f32_e32 v124, v126, v127
	v_pk_fma_f32 v[14:15], v[44:45], v[120:121], v[14:15] op_sel:[0,1,0]
	v_add_f32_e32 v130, v128, v129
	v_add_f32_dpp v124, v124, v124 quad_perm:[1,0,3,2] row_mask:0xf bank_mask:0xf bound_ctrl:1
	v_pk_fma_f32 v[16:17], v[46:47], v[120:121], v[16:17] op_sel:[0,1,0]
	ds_read_b128 v[100:103], v18 offset:6912
	v_add_f32_dpp v124, v124, v124 quad_perm:[2,3,0,1] row_mask:0xf bank_mask:0xf bound_ctrl:1
	ds_read_b128 v[108:111], v18 offset:31488
	ds_read_b128 v[116:119], v18 offset:23296
	v_add_f32_dpp v124, v124, v124 row_half_mirror row_mask:0xf bank_mask:0xf bound_ctrl:1
	ds_read_b128 v[104:107], v18 offset:15104
	ds_read_b128 v[112:115], v18 offset:39680
	v_add_f32_dpp v124, v124, v124 row_mirror row_mask:0xf bank_mask:0xf bound_ctrl:1
	v_pk_fma_f32 v[14:15], v[40:41], v[124:125], v[14:15] op_sel_hi:[1,0,1] neg_lo:[0,1,0] neg_hi:[0,1,0]
	v_pk_fma_f32 v[16:17], v[42:43], v[124:125], v[16:17] op_sel_hi:[1,0,1] neg_lo:[0,1,0] neg_hi:[0,1,0]
	v_add_f32_dpp v133, v131, v131 row_mirror row_mask:0xf bank_mask:0xc bound_ctrl:1
	v_add_f32_dpp v135, v132, v132 row_half_mirror row_mask:0xf bank_mask:0x5 bound_ctrl:1
	s_waitcnt lgkmcnt(6)
	v_pk_mul_f32 v[126:127], v[14:15], v[52:53]
	v_pk_mul_f32 v[128:129], v[14:15], v[48:49]
	v_pk_fma_f32 v[126:127], v[16:17], v[54:55], v[126:127]
	v_pk_fma_f32 v[128:129], v[16:17], v[50:51], v[128:129]
	v_add_f32_e32 v124, v126, v127
	v_pk_fma_f32 v[14:15], v[60:61], v[122:123], v[14:15] op_sel_hi:[1,0,1]
	v_add_f32_e32 v131, v128, v129
	v_add_f32_dpp v124, v124, v124 quad_perm:[1,0,3,2] row_mask:0xf bank_mask:0xf bound_ctrl:1
	v_pk_fma_f32 v[16:17], v[62:63], v[122:123], v[16:17] op_sel_hi:[1,0,1]
	ds_read_b128 v[20:23], v18 offset:7168
	v_add_f32_dpp v124, v124, v124 quad_perm:[2,3,0,1] row_mask:0xf bank_mask:0xf bound_ctrl:1
	ds_read_b128 v[28:31], v18 offset:31744
	ds_read2_b32 v[120:121], v3 offset0:192 offset1:208
	v_add_f32_dpp v124, v124, v124 row_half_mirror row_mask:0xf bank_mask:0xf bound_ctrl:1
	ds_read_b128 v[24:27], v18 offset:15360
	ds_read_b128 v[32:35], v18 offset:39936
	v_add_f32_dpp v124, v124, v124 row_mirror row_mask:0xf bank_mask:0xf bound_ctrl:1
	v_pk_fma_f32 v[14:15], v[56:57], v[124:125], v[14:15] op_sel_hi:[1,0,1] neg_lo:[0,1,0] neg_hi:[0,1,0]
	v_pk_fma_f32 v[16:17], v[58:59], v[124:125], v[16:17] op_sel_hi:[1,0,1] neg_lo:[0,1,0] neg_hi:[0,1,0]
	v_add_f32_dpp v135, v133, v133 row_half_mirror row_mask:0xf bank_mask:0xa bound_ctrl:1
	v_add_f32_dpp v138, v134, v134 quad_perm:[2,3,0,1] row_mask:0xf bank_mask:0xf bound_ctrl:1
	s_nop 0
	v_add_f32_dpp v98, v135, v135 quad_perm:[2,3,0,1] row_mask:0xf bank_mask:0xf bound_ctrl:1
	v_cndmask_b32_e64 v136, v138, v98, s[14:15]
	v_add_f32_dpp v132, v130, v130 row_mirror row_mask:0xf bank_mask:0x3 bound_ctrl:1
	s_waitcnt lgkmcnt(6)
	v_pk_mul_f32 v[126:127], v[14:15], v[100:101]
	v_pk_mul_f32 v[128:129], v[14:15], v[64:65]
	v_pk_fma_f32 v[126:127], v[16:17], v[102:103], v[126:127]
	v_pk_fma_f32 v[128:129], v[16:17], v[66:67], v[128:129]
	v_add_f32_e32 v124, v126, v127
	v_pk_fma_f32 v[14:15], v[108:109], v[122:123], v[14:15] op_sel:[0,1,0]
	v_add_f32_e32 v130, v128, v129
	v_add_f32_dpp v124, v124, v124 quad_perm:[1,0,3,2] row_mask:0xf bank_mask:0xf bound_ctrl:1
	v_pk_fma_f32 v[16:17], v[110:111], v[122:123], v[16:17] op_sel:[0,1,0]
	ds_read_b128 v[36:39], v18 offset:7424
	v_add_f32_dpp v124, v124, v124 quad_perm:[2,3,0,1] row_mask:0xf bank_mask:0xf bound_ctrl:1
	ds_read_b128 v[44:47], v18 offset:32000
	ds_read_b128 v[40:43], v18 offset:15616
	v_add_f32_dpp v124, v124, v124 row_half_mirror row_mask:0xf bank_mask:0xf bound_ctrl:1
	ds_read_b128 v[48:51], v18 offset:40192
	v_add_f32_dpp v132, v131, v131 row_mirror row_mask:0xf bank_mask:0xc bound_ctrl:1
	v_add_f32_dpp v124, v124, v124 row_mirror row_mask:0xf bank_mask:0xf bound_ctrl:1
	v_pk_fma_f32 v[14:15], v[104:105], v[124:125], v[14:15] op_sel_hi:[1,0,1] neg_lo:[0,1,0] neg_hi:[0,1,0]
	v_pk_fma_f32 v[16:17], v[106:107], v[124:125], v[16:17] op_sel_hi:[1,0,1] neg_lo:[0,1,0] neg_hi:[0,1,0]
	v_pk_mul_f32 v[14:15], v[14:15], v[116:117]
	v_pk_mul_f32 v[16:17], v[16:17], v[118:119]
	s_waitcnt lgkmcnt(5)
	v_pk_mul_f32 v[126:127], v[14:15], v[20:21]
	v_pk_mul_f32 v[128:129], v[14:15], v[112:113]
	v_pk_fma_f32 v[126:127], v[16:17], v[22:23], v[126:127]
	v_pk_fma_f32 v[128:129], v[16:17], v[114:115], v[128:129]
	v_add_f32_e32 v124, v126, v127
	v_pk_fma_f32 v[14:15], v[28:29], v[120:121], v[14:15] op_sel_hi:[1,0,1]
	v_add_f32_e32 v131, v128, v129
	v_add_f32_dpp v124, v124, v124 quad_perm:[1,0,3,2] row_mask:0xf bank_mask:0xf bound_ctrl:1
	v_pk_fma_f32 v[16:17], v[30:31], v[120:121], v[16:17] op_sel_hi:[1,0,1]
	ds_read_b128 v[52:55], v18 offset:7680
	v_add_f32_dpp v124, v124, v124 quad_perm:[2,3,0,1] row_mask:0xf bank_mask:0xf bound_ctrl:1
	ds_read_b128 v[60:63], v18 offset:32256
	ds_read2_b32 v[122:123], v3 offset0:224 offset1:240
	v_add_f32_dpp v124, v124, v124 row_half_mirror row_mask:0xf bank_mask:0xf bound_ctrl:1
	ds_read_b128 v[56:59], v18 offset:15872
	ds_read_b128 v[64:67], v18 offset:40448
	v_add_f32_dpp v124, v124, v124 row_mirror row_mask:0xf bank_mask:0xf bound_ctrl:1
	v_pk_fma_f32 v[14:15], v[24:25], v[124:125], v[14:15] op_sel_hi:[1,0,1] neg_lo:[0,1,0] neg_hi:[0,1,0]
	v_pk_fma_f32 v[16:17], v[26:27], v[124:125], v[16:17] op_sel_hi:[1,0,1] neg_lo:[0,1,0] neg_hi:[0,1,0]
	v_add_f32_dpp v133, v130, v130 row_mirror row_mask:0xf bank_mask:0x3 bound_ctrl:1
	s_waitcnt lgkmcnt(6)
	v_pk_mul_f32 v[126:127], v[14:15], v[36:37]
	v_pk_mul_f32 v[128:129], v[14:15], v[32:33]
	v_pk_fma_f32 v[126:127], v[16:17], v[38:39], v[126:127]
	v_pk_fma_f32 v[128:129], v[16:17], v[34:35], v[128:129]
	v_add_f32_e32 v124, v126, v127
	v_pk_fma_f32 v[14:15], v[44:45], v[120:121], v[14:15] op_sel:[0,1,0]
	v_add_f32_e32 v130, v128, v129
	v_add_f32_dpp v124, v124, v124 quad_perm:[1,0,3,2] row_mask:0xf bank_mask:0xf bound_ctrl:1
	v_pk_fma_f32 v[16:17], v[46:47], v[120:121], v[16:17] op_sel:[0,1,0]
	ds_read_b128 v[100:103], v18 offset:7936
	v_add_f32_dpp v124, v124, v124 quad_perm:[2,3,0,1] row_mask:0xf bank_mask:0xf bound_ctrl:1
	ds_read_b128 v[108:111], v18 offset:32512
	ds_read_b128 v[116:119], v18 offset:24320
	v_add_f32_dpp v124, v124, v124 row_half_mirror row_mask:0xf bank_mask:0xf bound_ctrl:1
	ds_read_b128 v[104:107], v18 offset:16128
	ds_read_b128 v[112:115], v18 offset:40704
	v_add_f32_dpp v124, v124, v124 row_mirror row_mask:0xf bank_mask:0xf bound_ctrl:1
	v_pk_fma_f32 v[14:15], v[40:41], v[124:125], v[14:15] op_sel_hi:[1,0,1] neg_lo:[0,1,0] neg_hi:[0,1,0]
	v_pk_fma_f32 v[16:17], v[42:43], v[124:125], v[16:17] op_sel_hi:[1,0,1] neg_lo:[0,1,0] neg_hi:[0,1,0]
	v_add_f32_dpp v133, v131, v131 row_mirror row_mask:0xf bank_mask:0xc bound_ctrl:1
	v_add_f32_dpp v134, v132, v132 row_half_mirror row_mask:0xf bank_mask:0x5 bound_ctrl:1
	s_waitcnt lgkmcnt(6)
	v_pk_mul_f32 v[126:127], v[14:15], v[52:53]
	v_pk_mul_f32 v[128:129], v[14:15], v[48:49]
	v_pk_fma_f32 v[126:127], v[16:17], v[54:55], v[126:127]
	v_pk_fma_f32 v[128:129], v[16:17], v[50:51], v[128:129]
	v_add_f32_e32 v124, v126, v127
	v_pk_fma_f32 v[14:15], v[60:61], v[122:123], v[14:15] op_sel_hi:[1,0,1]
	v_add_f32_e32 v131, v128, v129
	v_add_f32_dpp v124, v124, v124 quad_perm:[1,0,3,2] row_mask:0xf bank_mask:0xf bound_ctrl:1
	v_pk_fma_f32 v[16:17], v[62:63], v[122:123], v[16:17] op_sel_hi:[1,0,1]
	ds_read_b128 v[20:23], v68
	v_add_f32_dpp v124, v124, v124 quad_perm:[2,3,0,1] row_mask:0xf bank_mask:0xf bound_ctrl:1
	ds_read_b128 v[28:31], v68 offset:24576
	ds_read2_b32 v[120:121], v69 offset1:16
	v_add_f32_dpp v124, v124, v124 row_half_mirror row_mask:0xf bank_mask:0xf bound_ctrl:1
	ds_read_b128 v[24:27], v68 offset:8192
	ds_read_b128 v[32:35], v68 offset:32768
	v_add_f32_dpp v124, v124, v124 row_mirror row_mask:0xf bank_mask:0xf bound_ctrl:1
	v_pk_fma_f32 v[14:15], v[56:57], v[124:125], v[14:15] op_sel_hi:[1,0,1] neg_lo:[0,1,0] neg_hi:[0,1,0]
	v_pk_fma_f32 v[16:17], v[58:59], v[124:125], v[16:17] op_sel_hi:[1,0,1] neg_lo:[0,1,0] neg_hi:[0,1,0]
	v_add_f32_dpp v134, v133, v133 row_half_mirror row_mask:0xf bank_mask:0xa bound_ctrl:1
	v_add_f32_dpp v132, v130, v130 row_mirror row_mask:0xf bank_mask:0x3 bound_ctrl:1
	s_waitcnt lgkmcnt(6)
	v_pk_mul_f32 v[126:127], v[14:15], v[100:101]
	v_pk_mul_f32 v[128:129], v[14:15], v[64:65]
	v_pk_fma_f32 v[126:127], v[16:17], v[102:103], v[126:127]
	v_pk_fma_f32 v[128:129], v[16:17], v[66:67], v[128:129]
	v_add_f32_e32 v124, v126, v127
	v_pk_fma_f32 v[14:15], v[108:109], v[122:123], v[14:15] op_sel:[0,1,0]
	v_add_f32_e32 v130, v128, v129
	v_add_f32_dpp v124, v124, v124 quad_perm:[1,0,3,2] row_mask:0xf bank_mask:0xf bound_ctrl:1
	v_pk_fma_f32 v[16:17], v[110:111], v[122:123], v[16:17] op_sel:[0,1,0]
	ds_read_b128 v[36:39], v68 offset:256
	v_add_f32_dpp v124, v124, v124 quad_perm:[2,3,0,1] row_mask:0xf bank_mask:0xf bound_ctrl:1
	ds_read_b128 v[44:47], v68 offset:24832
	ds_read_b128 v[40:43], v68 offset:8448
	v_add_f32_dpp v124, v124, v124 row_half_mirror row_mask:0xf bank_mask:0xf bound_ctrl:1
	ds_read_b128 v[48:51], v68 offset:33024
	v_add_f32_dpp v132, v131, v131 row_mirror row_mask:0xf bank_mask:0xc bound_ctrl:1
	v_add_f32_dpp v124, v124, v124 row_mirror row_mask:0xf bank_mask:0xf bound_ctrl:1
	v_pk_fma_f32 v[14:15], v[104:105], v[124:125], v[14:15] op_sel_hi:[1,0,1] neg_lo:[0,1,0] neg_hi:[0,1,0]
	v_pk_fma_f32 v[16:17], v[106:107], v[124:125], v[16:17] op_sel_hi:[1,0,1] neg_lo:[0,1,0] neg_hi:[0,1,0]
	v_pk_mul_f32 v[14:15], v[14:15], v[116:117]
	v_pk_mul_f32 v[16:17], v[16:17], v[118:119]
	s_add_i32 s8, s8, 1
	s_add_i32 s71, s71, 32
	s_cmpk_lg_i32 s8, 0x88
	s_barrier
	s_cbranch_scc0 .LBB0_618
	s_add_i32 s33, s33, 0xa800
	s_cmp_eq_u32 s33, 0x1f800
	s_cselect_b32 s33, 0, s33
	s_add_i32 s19, s19, s20
	s_cmp_eq_u32 s8, 8
	s_cselect_b32 s19, s21, s19
	s_mov_b32 s46, s19
	s_branch .Lsc_body
